# v88 + Gray-code MFMA issue order in the three K-loops (every second A-pair swapped: one operand changes per MFMA)
# baseline (speedup 1.0000x reference)
; #define PG8_STAGEA(bufoff, soff, voff) do { _Pragma("unroll") for (int _i = 0; _i < 2; ++_i) \
;         __builtin_amdgcn_raw_ptr_buffer_load_lds(rsA, (PG8_LAS unsigned*)(lds + (bufoff) + ldsw + _i * 8192), 16, (voff)[_i], (soff), 0, 0); } while (0)
; #define PG8_STAGEB(bufoff, soff, voff) do { _Pragma("unroll") for (int _i = 0; _i < 2; ++_i) \
;         __builtin_amdgcn_raw_ptr_buffer_load_lds(rsB, (PG8_LAS unsigned*)(lds + (bufoff) + ldsw + _i * 8192), 16, (voff)[_i], (soff), 0, 0); } while (0)
; #define PG8_LDA(dst, b, h) do { _Pragma("unroll") for (int m = 0; m < 4; ++m) _Pragma("unroll") for (int k = 0; k < 2; ++k) dst[m][k] = *(const PG8_LAS bf16x8*)(lds + PG8_SA(b, h) + aoff + m * 2048 + k * 1024); } while (0)
; #define PG8_LDB(dst, b, h) do { _Pragma("unroll") for (int n = 0; n < 2; ++n) _Pragma("unroll") for (int k = 0; k < 2; ++k) dst[n][k] = *(const PG8_LAS bf16x8*)(lds + PG8_SB(b, h) + boff + n * 2048 + k * 1024); } while (0)
; #define PG8_MMA(ai, bj, At, Bt) do { __builtin_amdgcn_s_setprio(1); _Pragma("unroll") for (int m = 0; m < 4; ++m) _Pragma("unroll") for (int n = 0; n < 2; ++n) _Pragma("unroll") for (int k = 0; k < 2; ++k) \
;         acc[ai][bj][m][n] = __builtin_amdgcn_mfma_f32_16x16x32_bf16(Bt[n][k], At[m][k], acc[ai][bj][m][n], 0, 0, 0); __builtin_amdgcn_s_setprio(0); } while (0)
; #define PG8_WAIT_V(n) asm volatile("s_waitcnt vmcnt(" #n ")" ::: "memory")
; #define PG8_WAIT_L(n) asm volatile("s_waitcnt lgkmcnt(" #n ")" ::: "memory")
; #define PG8_BAR __builtin_amdgcn_s_barrier()
; #define PG8_SCHED __builtin_amdgcn_sched_barrier(0)
; template <class Epi, class Sched, bool ALIGN_EPI = false>
; __device__ __forceinline__ void gemm_phase(PG8_LAS unsigned char* lds, const Gemm g, const Sched& S, const Epi& E, const int tid) {
;     ...
;             PG8_LDB(B0, 0, 0); PG8_LDB(B1, 0, 1); PG8_SCHED; PG8_LDA(At, 0, 0); PG8_STAGEA(PG8_SA(1, 1), a1 + hstepA, voffA);
;             PG8_WAIT_V(8); PG8_WAIT_L(0); PG8_BAR; PG8_MMA(0, 0, At, B0); PG8_MMA(0, 1, At, B1); PG8_BAR; PG8_SCHED;
;             PG8_LDA(At, 0, 1); PG8_STAGEB(PG8_SB(0, 0), b2, voffB); PG8_STAGEB(PG8_SB(0, 1), b2 + hstepB, voffB); PG8_STAGEA(PG8_SA(0, 0), a2, voffA);
;             PG8_WAIT_V(8); PG8_WAIT_L(0); PG8_BAR; PG8_MMA(1, 0, At, B0); PG8_MMA(1, 1, At, B1); PG8_BAR; PG8_SCHED;
.LBB0_307:
	v_add_u32_e32 v130, 0x10000, v137
	ds_read_b128 v[144:147], v130
	ds_read_b128 v[148:151], v130 offset:1024
	ds_read_b128 v[164:167], v130 offset:2048
	ds_read_b128 v[168:171], v130 offset:3072
	v_add_u32_e32 v130, 0x14000, v137
	ds_read_b128 v[172:175], v130
	ds_read_b128 v[176:179], v130 offset:1024
	ds_read_b128 v[180:183], v130 offset:2048
	ds_read_b128 v[184:187], v130 offset:3072
	s_add_i32 s38, s19, 0xfff80080
	s_cmp_eq_u32 s37, 28
	s_cselect_b32 s42, s18, s38
	s_cselect_b32 s39, s31, s36
	s_or_b32 s38, s42, 0x80
	s_mov_b32 m0, s26
	ds_read_b128 v[188:191], v138
	ds_read_b128 v[202:205], v138 offset:1024
	ds_read_b128 v[206:209], v138 offset:2048
	ds_read_b128 v[210:213], v138 offset:3072
	ds_read_b128 v[214:217], v138 offset:4096
	ds_read_b128 v[218:221], v138 offset:5120
	ds_read_b128 v[222:225], v138 offset:6144
	ds_read_b128 v[226:229], v138 offset:7168
	buffer_load_dwordx4 v0, s[88:91], s19 offen lds
	s_mov_b32 m0, s27
	s_nop 0
	buffer_load_dwordx4 v133, s[88:91], s19 offen lds
	s_waitcnt vmcnt(8)
	s_waitcnt lgkmcnt(0)
	s_barrier
	s_setprio 1
	s_waitcnt lgkmcnt(7)
	v_mfma_f32_16x16x32_bf16 v[126:129], v[144:147], v[188:191], v[126:129]
	v_mfma_f32_16x16x32_bf16 v[118:121], v[164:167], v[188:191], v[118:121]
	s_waitcnt lgkmcnt(5)
	v_mfma_f32_16x16x32_bf16 v[102:105], v[164:167], v[206:209], v[102:105]
	v_mfma_f32_16x16x32_bf16 v[110:113], v[144:147], v[206:209], v[110:113]
	s_waitcnt lgkmcnt(3)
	v_mfma_f32_16x16x32_bf16 v[94:97], v[144:147], v[214:217], v[94:97]
	v_mfma_f32_16x16x32_bf16 v[86:89], v[164:167], v[214:217], v[86:89]
	s_waitcnt lgkmcnt(1)
	v_mfma_f32_16x16x32_bf16 v[70:73], v[164:167], v[222:225], v[70:73]
	v_mfma_f32_16x16x32_bf16 v[78:81], v[144:147], v[222:225], v[78:81]
	v_mfma_f32_16x16x32_bf16 v[126:129], v[148:151], v[202:205], v[126:129]
	v_mfma_f32_16x16x32_bf16 v[118:121], v[168:171], v[202:205], v[118:121]
	v_mfma_f32_16x16x32_bf16 v[102:105], v[168:171], v[210:213], v[102:105]
	v_mfma_f32_16x16x32_bf16 v[110:113], v[148:151], v[210:213], v[110:113]
	v_mfma_f32_16x16x32_bf16 v[94:97], v[148:151], v[218:221], v[94:97]
	v_mfma_f32_16x16x32_bf16 v[86:89], v[168:171], v[218:221], v[86:89]
	s_waitcnt lgkmcnt(0)
	v_mfma_f32_16x16x32_bf16 v[70:73], v[168:171], v[226:229], v[70:73]
	v_mfma_f32_16x16x32_bf16 v[78:81], v[148:151], v[226:229], v[78:81]
	s_setprio 0
	s_setprio 1
	v_mfma_f32_16x16x32_bf16 v[122:125], v[172:175], v[188:191], v[122:125]
	v_mfma_f32_16x16x32_bf16 v[114:117], v[180:183], v[188:191], v[114:117]
	v_mfma_f32_16x16x32_bf16 v[98:101], v[180:183], v[206:209], v[98:101]
	v_mfma_f32_16x16x32_bf16 v[106:109], v[172:175], v[206:209], v[106:109]
	v_mfma_f32_16x16x32_bf16 v[90:93], v[172:175], v[214:217], v[90:93]
	v_mfma_f32_16x16x32_bf16 v[82:85], v[180:183], v[214:217], v[82:85]
	v_mfma_f32_16x16x32_bf16 v[66:69], v[180:183], v[222:225], v[66:69]
	v_mfma_f32_16x16x32_bf16 v[74:77], v[172:175], v[222:225], v[74:77]
	v_mfma_f32_16x16x32_bf16 v[122:125], v[176:179], v[202:205], v[122:125]
	v_mfma_f32_16x16x32_bf16 v[114:117], v[184:187], v[202:205], v[114:117]
	v_mfma_f32_16x16x32_bf16 v[98:101], v[184:187], v[210:213], v[98:101]
	v_mfma_f32_16x16x32_bf16 v[106:109], v[176:179], v[210:213], v[106:109]
	v_mfma_f32_16x16x32_bf16 v[90:93], v[176:179], v[218:221], v[90:93]
	v_mfma_f32_16x16x32_bf16 v[82:85], v[184:187], v[218:221], v[82:85]
	v_mfma_f32_16x16x32_bf16 v[66:69], v[184:187], v[226:229], v[66:69]
	v_mfma_f32_16x16x32_bf16 v[74:77], v[176:179], v[226:229], v[74:77]
	s_setprio 0
	s_barrier
	s_mov_b32 m0, s3
	s_mov_b32 s46, s90
	s_mov_b32 s47, s91
	ds_read_b128 v[188:191], v138 offset:16384
	ds_read_b128 v[202:205], v138 offset:17408
	ds_read_b128 v[206:209], v138 offset:18432
	ds_read_b128 v[210:213], v138 offset:19456
	ds_read_b128 v[214:217], v138 offset:20480
	ds_read_b128 v[218:221], v138 offset:21504
	ds_read_b128 v[222:225], v138 offset:22528
	ds_read_b128 v[226:229], v138 offset:23552
	buffer_load_dwordx4 v132, s[44:47], s39 offen lds
	s_mov_b32 m0, s7
	s_add_i32 s43, s39, 0x80000
	buffer_load_dwordx4 v134, s[44:47], s39 offen lds
	s_mov_b32 m0, s11
	s_nop 0
	buffer_load_dwordx4 v132, s[44:47], s43 offen lds
	s_mov_b32 m0, s14
	s_nop 0
	buffer_load_dwordx4 v134, s[44:47], s43 offen lds
	s_mov_b32 m0, s2
	s_nop 0
	buffer_load_dwordx4 v0, s[88:91], s42 offen lds
	s_mov_b32 m0, s15
	s_nop 0
	buffer_load_dwordx4 v133, s[88:91], s42 offen lds
	s_waitcnt vmcnt(8)
	s_waitcnt lgkmcnt(0)
	s_barrier
	s_setprio 1
	s_waitcnt lgkmcnt(7)
	v_mfma_f32_16x16x32_bf16 v[62:65], v[144:147], v[188:191], v[62:65]
	v_mfma_f32_16x16x32_bf16 v[54:57], v[164:167], v[188:191], v[54:57]
	s_waitcnt lgkmcnt(5)
	v_mfma_f32_16x16x32_bf16 v[38:41], v[164:167], v[206:209], v[38:41]
	v_mfma_f32_16x16x32_bf16 v[46:49], v[144:147], v[206:209], v[46:49]
	s_waitcnt lgkmcnt(3)
	v_mfma_f32_16x16x32_bf16 v[30:33], v[144:147], v[214:217], v[30:33]
	v_mfma_f32_16x16x32_bf16 v[22:25], v[164:167], v[214:217], v[22:25]
	s_waitcnt lgkmcnt(1)
	v_mfma_f32_16x16x32_bf16 v[6:9], v[164:167], v[222:225], v[6:9]
	v_mfma_f32_16x16x32_bf16 v[14:17], v[144:147], v[222:225], v[14:17]
	v_mfma_f32_16x16x32_bf16 v[62:65], v[148:151], v[202:205], v[62:65]
	v_mfma_f32_16x16x32_bf16 v[54:57], v[168:171], v[202:205], v[54:57]
	v_mfma_f32_16x16x32_bf16 v[38:41], v[168:171], v[210:213], v[38:41]
	v_mfma_f32_16x16x32_bf16 v[46:49], v[148:151], v[210:213], v[46:49]
	v_mfma_f32_16x16x32_bf16 v[30:33], v[148:151], v[218:221], v[30:33]
	v_mfma_f32_16x16x32_bf16 v[22:25], v[168:171], v[218:221], v[22:25]
	s_waitcnt lgkmcnt(0)
	v_mfma_f32_16x16x32_bf16 v[6:9], v[168:171], v[226:229], v[6:9]
	v_mfma_f32_16x16x32_bf16 v[14:17], v[148:151], v[226:229], v[14:17]
	s_setprio 0
	s_setprio 1
	v_mfma_f32_16x16x32_bf16 v[58:61], v[172:175], v[188:191], v[58:61]
	v_mfma_f32_16x16x32_bf16 v[50:53], v[180:183], v[188:191], v[50:53]
	v_mfma_f32_16x16x32_bf16 v[34:37], v[180:183], v[206:209], v[34:37]
	v_mfma_f32_16x16x32_bf16 v[42:45], v[172:175], v[206:209], v[42:45]
	v_mfma_f32_16x16x32_bf16 v[26:29], v[172:175], v[214:217], v[26:29]
	v_mfma_f32_16x16x32_bf16 v[18:21], v[180:183], v[214:217], v[18:21]
	v_mfma_f32_16x16x32_bf16 v[2:5], v[180:183], v[222:225], v[2:5]
	v_mfma_f32_16x16x32_bf16 v[10:13], v[172:175], v[222:225], v[10:13]
	v_mfma_f32_16x16x32_bf16 v[58:61], v[176:179], v[202:205], v[58:61]
	v_mfma_f32_16x16x32_bf16 v[50:53], v[184:187], v[202:205], v[50:53]
	v_mfma_f32_16x16x32_bf16 v[34:37], v[184:187], v[210:213], v[34:37]
	v_mfma_f32_16x16x32_bf16 v[42:45], v[176:179], v[210:213], v[42:45]
	v_mfma_f32_16x16x32_bf16 v[26:29], v[176:179], v[218:221], v[26:29]
	v_mfma_f32_16x16x32_bf16 v[18:21], v[184:187], v[218:221], v[18:21]
	v_mfma_f32_16x16x32_bf16 v[2:5], v[184:187], v[226:229], v[2:5]
	v_mfma_f32_16x16x32_bf16 v[10:13], v[176:179], v[226:229], v[10:13]
	s_setprio 0
	s_barrier
; #define PG8_STAGEA(bufoff, soff, voff) do { _Pragma("unroll") for (int _i = 0; _i < 2; ++_i) \
;         __builtin_amdgcn_raw_ptr_buffer_load_lds(rsA, (PG8_LAS unsigned*)(lds + (bufoff) + ldsw + _i * 8192), 16, (voff)[_i], (soff), 0, 0); } while (0)
; #define PG8_STAGEB(bufoff, soff, voff) do { _Pragma("unroll") for (int _i = 0; _i < 2; ++_i) \
;         __builtin_amdgcn_raw_ptr_buffer_load_lds(rsB, (PG8_LAS unsigned*)(lds + (bufoff) + ldsw + _i * 8192), 16, (voff)[_i], (soff), 0, 0); } while (0)
; #define PG8_LDA(dst, b, h) do { _Pragma("unroll") for (int m = 0; m < 4; ++m) _Pragma("unroll") for (int k = 0; k < 2; ++k) dst[m][k] = *(const PG8_LAS bf16x8*)(lds + PG8_SA(b, h) + aoff + m * 2048 + k * 1024); } while (0)
; #define PG8_LDB(dst, b, h) do { _Pragma("unroll") for (int n = 0; n < 2; ++n) _Pragma("unroll") for (int k = 0; k < 2; ++k) dst[n][k] = *(const PG8_LAS bf16x8*)(lds + PG8_SB(b, h) + boff + n * 2048 + k * 1024); } while (0)
; #define PG8_MMA(ai, bj, At, Bt) do { __builtin_amdgcn_s_setprio(1); _Pragma("unroll") for (int m = 0; m < 4; ++m) _Pragma("unroll") for (int n = 0; n < 2; ++n) _Pragma("unroll") for (int k = 0; k < 2; ++k) \
;         acc[ai][bj][m][n] = __builtin_amdgcn_mfma_f32_16x16x32_bf16(Bt[n][k], At[m][k], acc[ai][bj][m][n], 0, 0, 0); __builtin_amdgcn_s_setprio(0); } while (0)
; #define PG8_WAIT_V(n) asm volatile("s_waitcnt vmcnt(" #n ")" ::: "memory")
; #define PG8_WAIT_L(n) asm volatile("s_waitcnt lgkmcnt(" #n ")" ::: "memory")
; #define PG8_BAR __builtin_amdgcn_s_barrier()
; #define PG8_SCHED __builtin_amdgcn_sched_barrier(0)
; template <class Epi, class Sched, bool ALIGN_EPI = false>
; __device__ __forceinline__ void gemm_phase(PG8_LAS unsigned char* lds, const Gemm g, const Sched& S, const Epi& E, const int tid) {
;     ...
;             PG8_LDB(B0, 1, 0); PG8_LDB(B1, 1, 1); PG8_SCHED; PG8_LDA(At, 1, 0); PG8_STAGEA(PG8_SA(0, 1), a2 + hstepA, voffA);
;             PG8_WAIT_V(8); PG8_WAIT_L(0); PG8_BAR; PG8_MMA(0, 0, At, B0); PG8_MMA(0, 1, At, B1); PG8_BAR; PG8_SCHED;
;             PG8_LDA(At, 1, 1); PG8_STAGEB(PG8_SB(1, 0), b3, voffB); PG8_STAGEB(PG8_SB(1, 1), b3 + hstepB, voffB); PG8_STAGEA(PG8_SA(1, 0), a3, voffA);
;             PG8_WAIT_V(8); PG8_WAIT_L(0); PG8_BAR; PG8_MMA(1, 0, At, B0); PG8_MMA(1, 1, At, B1); PG8_BAR; PG8_SCHED;
;         }
	v_add_u32_e32 v130, 0x18000, v137
	ds_read_b128 v[144:147], v130
	ds_read_b128 v[148:151], v130 offset:1024
	ds_read_b128 v[164:167], v130 offset:2048
	ds_read_b128 v[168:171], v130 offset:3072
	v_add_u32_e32 v130, 0x1c000, v137
	ds_read_b128 v[172:175], v130
	ds_read_b128 v[176:179], v130 offset:1024
	ds_read_b128 v[180:183], v130 offset:2048
	ds_read_b128 v[184:187], v130 offset:3072
	s_add_i32 s42, s42, 0x80000
	s_mov_b32 m0, s16
	ds_read_b128 v[188:191], v138 offset:32768
	ds_read_b128 v[202:205], v138 offset:33792
	ds_read_b128 v[206:209], v138 offset:34816
	ds_read_b128 v[210:213], v138 offset:35840
	ds_read_b128 v[214:217], v138 offset:36864
	ds_read_b128 v[218:221], v138 offset:37888
	ds_read_b128 v[222:225], v138 offset:38912
	ds_read_b128 v[226:229], v138 offset:39936
	buffer_load_dwordx4 v0, s[88:91], s42 offen lds
	s_mov_b32 m0, s17
	s_nop 0
	buffer_load_dwordx4 v133, s[88:91], s42 offen lds
	s_waitcnt vmcnt(8)
	s_waitcnt lgkmcnt(0)
	s_barrier
	s_setprio 1
	s_waitcnt lgkmcnt(7)
	v_mfma_f32_16x16x32_bf16 v[126:129], v[144:147], v[188:191], v[126:129]
	v_mfma_f32_16x16x32_bf16 v[118:121], v[164:167], v[188:191], v[118:121]
	s_waitcnt lgkmcnt(5)
	v_mfma_f32_16x16x32_bf16 v[102:105], v[164:167], v[206:209], v[102:105]
	v_mfma_f32_16x16x32_bf16 v[110:113], v[144:147], v[206:209], v[110:113]
	s_waitcnt lgkmcnt(3)
	v_mfma_f32_16x16x32_bf16 v[94:97], v[144:147], v[214:217], v[94:97]
	v_mfma_f32_16x16x32_bf16 v[86:89], v[164:167], v[214:217], v[86:89]
	s_waitcnt lgkmcnt(1)
	v_mfma_f32_16x16x32_bf16 v[70:73], v[164:167], v[222:225], v[70:73]
	v_mfma_f32_16x16x32_bf16 v[78:81], v[144:147], v[222:225], v[78:81]
	v_mfma_f32_16x16x32_bf16 v[126:129], v[148:151], v[202:205], v[126:129]
	v_mfma_f32_16x16x32_bf16 v[118:121], v[168:171], v[202:205], v[118:121]
	v_mfma_f32_16x16x32_bf16 v[102:105], v[168:171], v[210:213], v[102:105]
	v_mfma_f32_16x16x32_bf16 v[110:113], v[148:151], v[210:213], v[110:113]
	v_mfma_f32_16x16x32_bf16 v[94:97], v[148:151], v[218:221], v[94:97]
	v_mfma_f32_16x16x32_bf16 v[86:89], v[168:171], v[218:221], v[86:89]
	s_waitcnt lgkmcnt(0)
	v_mfma_f32_16x16x32_bf16 v[70:73], v[168:171], v[226:229], v[70:73]
	v_mfma_f32_16x16x32_bf16 v[78:81], v[148:151], v[226:229], v[78:81]
	s_setprio 0
	s_setprio 1
	v_mfma_f32_16x16x32_bf16 v[122:125], v[172:175], v[188:191], v[122:125]
	v_mfma_f32_16x16x32_bf16 v[114:117], v[180:183], v[188:191], v[114:117]
	v_mfma_f32_16x16x32_bf16 v[98:101], v[180:183], v[206:209], v[98:101]
	v_mfma_f32_16x16x32_bf16 v[106:109], v[172:175], v[206:209], v[106:109]
	v_mfma_f32_16x16x32_bf16 v[90:93], v[172:175], v[214:217], v[90:93]
	v_mfma_f32_16x16x32_bf16 v[82:85], v[180:183], v[214:217], v[82:85]
	v_mfma_f32_16x16x32_bf16 v[66:69], v[180:183], v[222:225], v[66:69]
	v_mfma_f32_16x16x32_bf16 v[74:77], v[172:175], v[222:225], v[74:77]
	v_mfma_f32_16x16x32_bf16 v[122:125], v[176:179], v[202:205], v[122:125]
	v_mfma_f32_16x16x32_bf16 v[114:117], v[184:187], v[202:205], v[114:117]
	v_mfma_f32_16x16x32_bf16 v[98:101], v[184:187], v[210:213], v[98:101]
	v_mfma_f32_16x16x32_bf16 v[106:109], v[176:179], v[210:213], v[106:109]
	v_mfma_f32_16x16x32_bf16 v[90:93], v[176:179], v[218:221], v[90:93]
	v_mfma_f32_16x16x32_bf16 v[82:85], v[184:187], v[218:221], v[82:85]
	v_mfma_f32_16x16x32_bf16 v[66:69], v[184:187], v[226:229], v[66:69]
	v_mfma_f32_16x16x32_bf16 v[74:77], v[176:179], v[226:229], v[74:77]
	s_setprio 0
	s_barrier
	s_mov_b32 m0, s20
	s_or_b32 s42, s39, 0x80
	ds_read_b128 v[188:191], v138 offset:49152
	ds_read_b128 v[202:205], v138 offset:50176
	ds_read_b128 v[206:209], v138 offset:51200
	ds_read_b128 v[210:213], v138 offset:52224
	ds_read_b128 v[214:217], v138 offset:53248
	ds_read_b128 v[218:221], v138 offset:54272
	ds_read_b128 v[222:225], v138 offset:55296
	ds_read_b128 v[226:229], v138 offset:56320
	buffer_load_dwordx4 v132, s[44:47], s42 offen lds
	s_mov_b32 m0, s21
	s_add_i32 s39, s39, 0x80080
	buffer_load_dwordx4 v134, s[44:47], s42 offen lds
	s_mov_b32 m0, s24
	s_nop 0
	buffer_load_dwordx4 v132, s[44:47], s39 offen lds
	s_mov_b32 m0, s25
	s_nop 0
	buffer_load_dwordx4 v134, s[44:47], s39 offen lds
	s_mov_b32 m0, s22
	s_nop 0
	buffer_load_dwordx4 v0, s[88:91], s38 offen lds
	s_mov_b32 m0, s23
	s_nop 0
	buffer_load_dwordx4 v133, s[88:91], s38 offen lds
	s_waitcnt vmcnt(8)
	s_waitcnt lgkmcnt(0)
	s_barrier
	s_setprio 1
	s_waitcnt lgkmcnt(7)
	v_mfma_f32_16x16x32_bf16 v[62:65], v[144:147], v[188:191], v[62:65]
	v_mfma_f32_16x16x32_bf16 v[54:57], v[164:167], v[188:191], v[54:57]
	s_waitcnt lgkmcnt(5)
	v_mfma_f32_16x16x32_bf16 v[38:41], v[164:167], v[206:209], v[38:41]
	v_mfma_f32_16x16x32_bf16 v[46:49], v[144:147], v[206:209], v[46:49]
	s_waitcnt lgkmcnt(3)
	v_mfma_f32_16x16x32_bf16 v[30:33], v[144:147], v[214:217], v[30:33]
	v_mfma_f32_16x16x32_bf16 v[22:25], v[164:167], v[214:217], v[22:25]
	s_waitcnt lgkmcnt(1)
	v_mfma_f32_16x16x32_bf16 v[6:9], v[164:167], v[222:225], v[6:9]
	v_mfma_f32_16x16x32_bf16 v[14:17], v[144:147], v[222:225], v[14:17]
	v_mfma_f32_16x16x32_bf16 v[62:65], v[148:151], v[202:205], v[62:65]
	v_mfma_f32_16x16x32_bf16 v[54:57], v[168:171], v[202:205], v[54:57]
	v_mfma_f32_16x16x32_bf16 v[38:41], v[168:171], v[210:213], v[38:41]
	v_mfma_f32_16x16x32_bf16 v[46:49], v[148:151], v[210:213], v[46:49]
	v_mfma_f32_16x16x32_bf16 v[30:33], v[148:151], v[218:221], v[30:33]
	v_mfma_f32_16x16x32_bf16 v[22:25], v[168:171], v[218:221], v[22:25]
	s_waitcnt lgkmcnt(0)
	v_mfma_f32_16x16x32_bf16 v[6:9], v[168:171], v[226:229], v[6:9]
	v_mfma_f32_16x16x32_bf16 v[14:17], v[148:151], v[226:229], v[14:17]
	s_setprio 0
	s_setprio 1
	v_mfma_f32_16x16x32_bf16 v[58:61], v[172:175], v[188:191], v[58:61]
	v_mfma_f32_16x16x32_bf16 v[50:53], v[180:183], v[188:191], v[50:53]
	v_mfma_f32_16x16x32_bf16 v[34:37], v[180:183], v[206:209], v[34:37]
	v_mfma_f32_16x16x32_bf16 v[42:45], v[172:175], v[206:209], v[42:45]
	v_mfma_f32_16x16x32_bf16 v[26:29], v[172:175], v[214:217], v[26:29]
	v_mfma_f32_16x16x32_bf16 v[18:21], v[180:183], v[214:217], v[18:21]
	v_mfma_f32_16x16x32_bf16 v[2:5], v[180:183], v[222:225], v[2:5]
	v_mfma_f32_16x16x32_bf16 v[10:13], v[172:175], v[222:225], v[10:13]
	v_mfma_f32_16x16x32_bf16 v[58:61], v[176:179], v[202:205], v[58:61]
	v_mfma_f32_16x16x32_bf16 v[50:53], v[184:187], v[202:205], v[50:53]
	v_mfma_f32_16x16x32_bf16 v[34:37], v[184:187], v[210:213], v[34:37]
	v_mfma_f32_16x16x32_bf16 v[42:45], v[176:179], v[210:213], v[42:45]
	v_mfma_f32_16x16x32_bf16 v[26:29], v[176:179], v[218:221], v[26:29]
	v_mfma_f32_16x16x32_bf16 v[18:21], v[184:187], v[218:221], v[18:21]
	v_mfma_f32_16x16x32_bf16 v[2:5], v[184:187], v[226:229], v[2:5]
	v_mfma_f32_16x16x32_bf16 v[10:13], v[176:179], v[226:229], v[10:13]
	s_setprio 0
	s_barrier
	s_add_i32 s37, s37, 2
	s_addk_i32 s19, 0x100
	s_addk_i32 s36, 0x100
	s_cmp_gt_u32 s37, 29
	s_cbranch_scc0 .LBB0_307
	s_and_b64 vcc, exec, s[12:13]
	s_cbranch_vccz .LBB0_310
	s_barrier

; #define PG8_STAGEA(bufoff, soff, voff) do { _Pragma("unroll") for (int _i = 0; _i < 2; ++_i) \
;         __builtin_amdgcn_raw_ptr_buffer_load_lds(rsA, (PG8_LAS unsigned*)(lds + (bufoff) + ldsw + _i * 8192), 16, (voff)[_i], (soff), 0, 0); } while (0)
; #define PG8_STAGEB(bufoff, soff, voff) do { _Pragma("unroll") for (int _i = 0; _i < 2; ++_i) \
;         __builtin_amdgcn_raw_ptr_buffer_load_lds(rsB, (PG8_LAS unsigned*)(lds + (bufoff) + ldsw + _i * 8192), 16, (voff)[_i], (soff), 0, 0); } while (0)
; #define PG8_LDA(dst, b, h) do { _Pragma("unroll") for (int m = 0; m < 4; ++m) _Pragma("unroll") for (int k = 0; k < 2; ++k) dst[m][k] = *(const PG8_LAS bf16x8*)(lds + PG8_SA(b, h) + aoff + m * 2048 + k * 1024); } while (0)
; #define PG8_LDB(dst, b, h) do { _Pragma("unroll") for (int n = 0; n < 2; ++n) _Pragma("unroll") for (int k = 0; k < 2; ++k) dst[n][k] = *(const PG8_LAS bf16x8*)(lds + PG8_SB(b, h) + boff + n * 2048 + k * 1024); } while (0)
; #define PG8_MMA(ai, bj, At, Bt) do { __builtin_amdgcn_s_setprio(1); _Pragma("unroll") for (int m = 0; m < 4; ++m) _Pragma("unroll") for (int n = 0; n < 2; ++n) _Pragma("unroll") for (int k = 0; k < 2; ++k) \
;         acc[ai][bj][m][n] = __builtin_amdgcn_mfma_f32_16x16x32_bf16(Bt[n][k], At[m][k], acc[ai][bj][m][n], 0, 0, 0); __builtin_amdgcn_s_setprio(0); } while (0)
; #define PG8_WAIT_V(n) asm volatile("s_waitcnt vmcnt(" #n ")" ::: "memory")
; #define PG8_WAIT_L(n) asm volatile("s_waitcnt lgkmcnt(" #n ")" ::: "memory")
; #define PG8_BAR __builtin_amdgcn_s_barrier()
; #define PG8_SCHED __builtin_amdgcn_sched_barrier(0)
; template <class Epi, class Sched, bool ALIGN_EPI = false>
; __device__ __forceinline__ void gemm_phase(PG8_LAS unsigned char* lds, const Gemm g, const Sched& S, const Epi& E, const int tid) {
;     ...
;             PG8_LDB(B0, 0, 0); PG8_LDB(B1, 0, 1); PG8_SCHED; PG8_LDA(At, 0, 0); PG8_STAGEA(PG8_SA(1, 1), a1 + hstepA, voffA);
;             PG8_WAIT_V(8); PG8_WAIT_L(0); PG8_BAR; PG8_MMA(0, 0, At, B0); PG8_MMA(0, 1, At, B1); PG8_BAR; PG8_SCHED;
;             PG8_LDA(At, 0, 1); PG8_STAGEB(PG8_SB(0, 0), b2, voffB); PG8_STAGEB(PG8_SB(0, 1), b2 + hstepB, voffB); PG8_STAGEA(PG8_SA(0, 0), a2, voffA);
;             PG8_WAIT_V(8); PG8_WAIT_L(0); PG8_BAR; PG8_MMA(1, 0, At, B0); PG8_MMA(1, 1, At, B1); PG8_BAR; PG8_SCHED;
.LBB0_330:
	v_add_u32_e32 v0, 0x10000, v170
	ds_read_b128 v[130:133], v0
	ds_read_b128 v[134:137], v0 offset:1024
	ds_read_b128 v[138:141], v0 offset:2048
	ds_read_b128 v[150:153], v0 offset:3072
	v_add_u32_e32 v0, 0x14000, v170
	ds_read_b128 v[172:175], v0
	ds_read_b128 v[176:179], v0 offset:1024
	ds_read_b128 v[180:183], v0 offset:2048
	ds_read_b128 v[184:187], v0 offset:3072
	s_add_i32 s14, s1, 0xfff80080
	s_cmp_eq_u32 s13, 28
	s_cselect_b32 s16, s0, s14
	s_cselect_b32 s15, s58, s12
	s_or_b32 s14, s16, 0x80
	s_mov_b32 m0, s54
	ds_read_b128 v[188:191], v171
	ds_read_b128 v[202:205], v171 offset:1024
	ds_read_b128 v[206:209], v171 offset:2048
	ds_read_b128 v[210:213], v171 offset:3072
	ds_read_b128 v[214:217], v171 offset:4096
	ds_read_b128 v[218:221], v171 offset:5120
	ds_read_b128 v[222:225], v171 offset:6144
	ds_read_b128 v[226:229], v171 offset:7168
	buffer_load_dwordx4 v145, s[88:91], s1 offen lds
	s_mov_b32 m0, s55
	s_nop 0
	buffer_load_dwordx4 v167, s[88:91], s1 offen lds
	s_waitcnt vmcnt(8)
	s_waitcnt lgkmcnt(0)
	s_barrier
	s_setprio 1
	s_waitcnt lgkmcnt(7)
	v_mfma_f32_16x16x32_bf16 v[118:121], v[130:133], v[188:191], v[118:121]
	v_mfma_f32_16x16x32_bf16 v[102:105], v[138:141], v[188:191], v[102:105]
	s_waitcnt lgkmcnt(5)
	v_mfma_f32_16x16x32_bf16 v[98:101], v[138:141], v[206:209], v[98:101]
	v_mfma_f32_16x16x32_bf16 v[114:117], v[130:133], v[206:209], v[114:117]
	s_waitcnt lgkmcnt(3)
	v_mfma_f32_16x16x32_bf16 v[86:89], v[130:133], v[214:217], v[86:89]
	v_mfma_f32_16x16x32_bf16 v[70:73], v[138:141], v[214:217], v[70:73]
	s_waitcnt lgkmcnt(1)
	v_mfma_f32_16x16x32_bf16 v[66:69], v[138:141], v[222:225], v[66:69]
	v_mfma_f32_16x16x32_bf16 v[82:85], v[130:133], v[222:225], v[82:85]
	v_mfma_f32_16x16x32_bf16 v[118:121], v[134:137], v[202:205], v[118:121]
	v_mfma_f32_16x16x32_bf16 v[102:105], v[150:153], v[202:205], v[102:105]
	v_mfma_f32_16x16x32_bf16 v[98:101], v[150:153], v[210:213], v[98:101]
	v_mfma_f32_16x16x32_bf16 v[114:117], v[134:137], v[210:213], v[114:117]
	v_mfma_f32_16x16x32_bf16 v[86:89], v[134:137], v[218:221], v[86:89]
	v_mfma_f32_16x16x32_bf16 v[70:73], v[150:153], v[218:221], v[70:73]
	s_waitcnt lgkmcnt(0)
	v_mfma_f32_16x16x32_bf16 v[66:69], v[150:153], v[226:229], v[66:69]
	v_mfma_f32_16x16x32_bf16 v[82:85], v[134:137], v[226:229], v[82:85]
	s_setprio 0
	s_setprio 1
	v_mfma_f32_16x16x32_bf16 v[126:129], v[172:175], v[188:191], v[126:129]
	v_mfma_f32_16x16x32_bf16 v[110:113], v[180:183], v[188:191], v[110:113]
	v_mfma_f32_16x16x32_bf16 v[106:109], v[180:183], v[206:209], v[106:109]
	v_mfma_f32_16x16x32_bf16 v[122:125], v[172:175], v[206:209], v[122:125]
	v_mfma_f32_16x16x32_bf16 v[94:97], v[172:175], v[214:217], v[94:97]
	v_mfma_f32_16x16x32_bf16 v[78:81], v[180:183], v[214:217], v[78:81]
	v_mfma_f32_16x16x32_bf16 v[74:77], v[180:183], v[222:225], v[74:77]
	v_mfma_f32_16x16x32_bf16 v[90:93], v[172:175], v[222:225], v[90:93]
	v_mfma_f32_16x16x32_bf16 v[126:129], v[176:179], v[202:205], v[126:129]
	v_mfma_f32_16x16x32_bf16 v[110:113], v[184:187], v[202:205], v[110:113]
	v_mfma_f32_16x16x32_bf16 v[106:109], v[184:187], v[210:213], v[106:109]
	v_mfma_f32_16x16x32_bf16 v[122:125], v[176:179], v[210:213], v[122:125]
	v_mfma_f32_16x16x32_bf16 v[94:97], v[176:179], v[218:221], v[94:97]
	v_mfma_f32_16x16x32_bf16 v[78:81], v[184:187], v[218:221], v[78:81]
	v_mfma_f32_16x16x32_bf16 v[74:77], v[184:187], v[226:229], v[74:77]
	v_mfma_f32_16x16x32_bf16 v[90:93], v[176:179], v[226:229], v[90:93]
	s_setprio 0
	s_barrier
	s_mov_b32 m0, s28
	s_mov_b32 s50, s90
	s_mov_b32 s51, s91
	ds_read_b128 v[188:191], v171 offset:16384
	ds_read_b128 v[202:205], v171 offset:17408
	ds_read_b128 v[206:209], v171 offset:18432
	ds_read_b128 v[210:213], v171 offset:19456
	ds_read_b128 v[214:217], v171 offset:20480
	ds_read_b128 v[218:221], v171 offset:21504
	ds_read_b128 v[222:225], v171 offset:22528
	ds_read_b128 v[226:229], v171 offset:23552
	buffer_load_dwordx4 v166, s[48:51], s15 offen lds
	s_mov_b32 m0, s29
	s_add_i32 s17, s15, 0x80000
	buffer_load_dwordx4 v168, s[48:51], s15 offen lds
	s_mov_b32 m0, s70
	s_nop 0
	buffer_load_dwordx4 v166, s[48:51], s17 offen lds
	s_mov_b32 m0, s71
	s_nop 0
	buffer_load_dwordx4 v168, s[48:51], s17 offen lds
	s_mov_b32 m0, s27
	s_nop 0
	buffer_load_dwordx4 v145, s[88:91], s16 offen lds
	s_mov_b32 m0, s72
	s_nop 0
	buffer_load_dwordx4 v167, s[88:91], s16 offen lds
	s_waitcnt vmcnt(8)
	s_waitcnt lgkmcnt(0)
	s_barrier
	s_setprio 1
	s_waitcnt lgkmcnt(7)
	v_mfma_f32_16x16x32_bf16 v[54:57], v[130:133], v[188:191], v[54:57]
	v_mfma_f32_16x16x32_bf16 v[38:41], v[138:141], v[188:191], v[38:41]
	s_waitcnt lgkmcnt(5)
	v_mfma_f32_16x16x32_bf16 v[34:37], v[138:141], v[206:209], v[34:37]
	v_mfma_f32_16x16x32_bf16 v[50:53], v[130:133], v[206:209], v[50:53]
	s_waitcnt lgkmcnt(3)
	v_mfma_f32_16x16x32_bf16 v[22:25], v[130:133], v[214:217], v[22:25]
	v_mfma_f32_16x16x32_bf16 v[6:9], v[138:141], v[214:217], v[6:9]
	s_waitcnt lgkmcnt(1)
	v_mfma_f32_16x16x32_bf16 v[2:5], v[138:141], v[222:225], v[2:5]
	v_mfma_f32_16x16x32_bf16 v[18:21], v[130:133], v[222:225], v[18:21]
	v_mfma_f32_16x16x32_bf16 v[54:57], v[134:137], v[202:205], v[54:57]
	v_mfma_f32_16x16x32_bf16 v[38:41], v[150:153], v[202:205], v[38:41]
	v_mfma_f32_16x16x32_bf16 v[34:37], v[150:153], v[210:213], v[34:37]
	v_mfma_f32_16x16x32_bf16 v[50:53], v[134:137], v[210:213], v[50:53]
	v_mfma_f32_16x16x32_bf16 v[22:25], v[134:137], v[218:221], v[22:25]
	v_mfma_f32_16x16x32_bf16 v[6:9], v[150:153], v[218:221], v[6:9]
	s_waitcnt lgkmcnt(0)
	v_mfma_f32_16x16x32_bf16 v[2:5], v[150:153], v[226:229], v[2:5]
	v_mfma_f32_16x16x32_bf16 v[18:21], v[134:137], v[226:229], v[18:21]
	s_setprio 0
	s_setprio 1
	v_mfma_f32_16x16x32_bf16 v[62:65], v[172:175], v[188:191], v[62:65]
	v_mfma_f32_16x16x32_bf16 v[46:49], v[180:183], v[188:191], v[46:49]
	v_mfma_f32_16x16x32_bf16 v[42:45], v[180:183], v[206:209], v[42:45]
	v_mfma_f32_16x16x32_bf16 v[58:61], v[172:175], v[206:209], v[58:61]
	v_mfma_f32_16x16x32_bf16 v[30:33], v[172:175], v[214:217], v[30:33]
	v_mfma_f32_16x16x32_bf16 v[14:17], v[180:183], v[214:217], v[14:17]
	v_mfma_f32_16x16x32_bf16 v[10:13], v[180:183], v[222:225], v[10:13]
	v_mfma_f32_16x16x32_bf16 v[26:29], v[172:175], v[222:225], v[26:29]
	v_mfma_f32_16x16x32_bf16 v[62:65], v[176:179], v[202:205], v[62:65]
	v_mfma_f32_16x16x32_bf16 v[46:49], v[184:187], v[202:205], v[46:49]
	v_mfma_f32_16x16x32_bf16 v[42:45], v[184:187], v[210:213], v[42:45]
	v_mfma_f32_16x16x32_bf16 v[58:61], v[176:179], v[210:213], v[58:61]
	v_mfma_f32_16x16x32_bf16 v[30:33], v[176:179], v[218:221], v[30:33]
	v_mfma_f32_16x16x32_bf16 v[14:17], v[184:187], v[218:221], v[14:17]
	v_mfma_f32_16x16x32_bf16 v[10:13], v[184:187], v[226:229], v[10:13]
	v_mfma_f32_16x16x32_bf16 v[26:29], v[176:179], v[226:229], v[26:29]
	s_setprio 0
	s_barrier
; #define PG8_STAGEA(bufoff, soff, voff) do { _Pragma("unroll") for (int _i = 0; _i < 2; ++_i) \
;         __builtin_amdgcn_raw_ptr_buffer_load_lds(rsA, (PG8_LAS unsigned*)(lds + (bufoff) + ldsw + _i * 8192), 16, (voff)[_i], (soff), 0, 0); } while (0)
; #define PG8_STAGEB(bufoff, soff, voff) do { _Pragma("unroll") for (int _i = 0; _i < 2; ++_i) \
;         __builtin_amdgcn_raw_ptr_buffer_load_lds(rsB, (PG8_LAS unsigned*)(lds + (bufoff) + ldsw + _i * 8192), 16, (voff)[_i], (soff), 0, 0); } while (0)
; #define PG8_LDA(dst, b, h) do { _Pragma("unroll") for (int m = 0; m < 4; ++m) _Pragma("unroll") for (int k = 0; k < 2; ++k) dst[m][k] = *(const PG8_LAS bf16x8*)(lds + PG8_SA(b, h) + aoff + m * 2048 + k * 1024); } while (0)
; #define PG8_LDB(dst, b, h) do { _Pragma("unroll") for (int n = 0; n < 2; ++n) _Pragma("unroll") for (int k = 0; k < 2; ++k) dst[n][k] = *(const PG8_LAS bf16x8*)(lds + PG8_SB(b, h) + boff + n * 2048 + k * 1024); } while (0)
; #define PG8_MMA(ai, bj, At, Bt) do { __builtin_amdgcn_s_setprio(1); _Pragma("unroll") for (int m = 0; m < 4; ++m) _Pragma("unroll") for (int n = 0; n < 2; ++n) _Pragma("unroll") for (int k = 0; k < 2; ++k) \
;         acc[ai][bj][m][n] = __builtin_amdgcn_mfma_f32_16x16x32_bf16(Bt[n][k], At[m][k], acc[ai][bj][m][n], 0, 0, 0); __builtin_amdgcn_s_setprio(0); } while (0)
; #define PG8_WAIT_V(n) asm volatile("s_waitcnt vmcnt(" #n ")" ::: "memory")
; #define PG8_WAIT_L(n) asm volatile("s_waitcnt lgkmcnt(" #n ")" ::: "memory")
; #define PG8_BAR __builtin_amdgcn_s_barrier()
; #define PG8_SCHED __builtin_amdgcn_sched_barrier(0)
; template <class Epi, class Sched, bool ALIGN_EPI = false>
; __device__ __forceinline__ void gemm_phase(PG8_LAS unsigned char* lds, const Gemm g, const Sched& S, const Epi& E, const int tid) {
;     ...
;             PG8_LDB(B0, 1, 0); PG8_LDB(B1, 1, 1); PG8_SCHED; PG8_LDA(At, 1, 0); PG8_STAGEA(PG8_SA(0, 1), a2 + hstepA, voffA);
;             PG8_WAIT_V(8); PG8_WAIT_L(0); PG8_BAR; PG8_MMA(0, 0, At, B0); PG8_MMA(0, 1, At, B1); PG8_BAR; PG8_SCHED;
;             PG8_LDA(At, 1, 1); PG8_STAGEB(PG8_SB(1, 0), b3, voffB); PG8_STAGEB(PG8_SB(1, 1), b3 + hstepB, voffB); PG8_STAGEA(PG8_SA(1, 0), a3, voffA);
;             PG8_WAIT_V(8); PG8_WAIT_L(0); PG8_BAR; PG8_MMA(1, 0, At, B0); PG8_MMA(1, 1, At, B1); PG8_BAR; PG8_SCHED;
;         }
	v_add_u32_e32 v0, 0x18000, v170
	ds_read_b128 v[130:133], v0
	ds_read_b128 v[134:137], v0 offset:1024
	ds_read_b128 v[138:141], v0 offset:2048
	ds_read_b128 v[150:153], v0 offset:3072
	v_add_u32_e32 v0, 0x1c000, v170
	ds_read_b128 v[172:175], v0
	ds_read_b128 v[176:179], v0 offset:1024
	ds_read_b128 v[180:183], v0 offset:2048
	ds_read_b128 v[184:187], v0 offset:3072
	s_add_i32 s16, s16, 0x80000
	s_mov_b32 m0, s73
	ds_read_b128 v[188:191], v171 offset:32768
	ds_read_b128 v[202:205], v171 offset:33792
	ds_read_b128 v[206:209], v171 offset:34816
	ds_read_b128 v[210:213], v171 offset:35840
	ds_read_b128 v[214:217], v171 offset:36864
	ds_read_b128 v[218:221], v171 offset:37888
	ds_read_b128 v[222:225], v171 offset:38912
	ds_read_b128 v[226:229], v171 offset:39936
	buffer_load_dwordx4 v145, s[88:91], s16 offen lds
	s_mov_b32 m0, s74
	s_nop 0
	buffer_load_dwordx4 v167, s[88:91], s16 offen lds
	s_waitcnt vmcnt(8)
	s_waitcnt lgkmcnt(0)
	s_barrier
	s_setprio 1
	s_waitcnt lgkmcnt(7)
	v_mfma_f32_16x16x32_bf16 v[118:121], v[130:133], v[188:191], v[118:121]
	v_mfma_f32_16x16x32_bf16 v[102:105], v[138:141], v[188:191], v[102:105]
	s_waitcnt lgkmcnt(5)
	v_mfma_f32_16x16x32_bf16 v[98:101], v[138:141], v[206:209], v[98:101]
	v_mfma_f32_16x16x32_bf16 v[114:117], v[130:133], v[206:209], v[114:117]
	s_waitcnt lgkmcnt(3)
	v_mfma_f32_16x16x32_bf16 v[86:89], v[130:133], v[214:217], v[86:89]
	v_mfma_f32_16x16x32_bf16 v[70:73], v[138:141], v[214:217], v[70:73]
	s_waitcnt lgkmcnt(1)
	v_mfma_f32_16x16x32_bf16 v[66:69], v[138:141], v[222:225], v[66:69]
	v_mfma_f32_16x16x32_bf16 v[82:85], v[130:133], v[222:225], v[82:85]
	v_mfma_f32_16x16x32_bf16 v[118:121], v[134:137], v[202:205], v[118:121]
	v_mfma_f32_16x16x32_bf16 v[102:105], v[150:153], v[202:205], v[102:105]
	v_mfma_f32_16x16x32_bf16 v[98:101], v[150:153], v[210:213], v[98:101]
	v_mfma_f32_16x16x32_bf16 v[114:117], v[134:137], v[210:213], v[114:117]
	v_mfma_f32_16x16x32_bf16 v[86:89], v[134:137], v[218:221], v[86:89]
	v_mfma_f32_16x16x32_bf16 v[70:73], v[150:153], v[218:221], v[70:73]
	s_waitcnt lgkmcnt(0)
	v_mfma_f32_16x16x32_bf16 v[66:69], v[150:153], v[226:229], v[66:69]
	v_mfma_f32_16x16x32_bf16 v[82:85], v[134:137], v[226:229], v[82:85]
	s_setprio 0
	s_setprio 1
	v_mfma_f32_16x16x32_bf16 v[126:129], v[172:175], v[188:191], v[126:129]
	v_mfma_f32_16x16x32_bf16 v[110:113], v[180:183], v[188:191], v[110:113]
	v_mfma_f32_16x16x32_bf16 v[106:109], v[180:183], v[206:209], v[106:109]
	v_mfma_f32_16x16x32_bf16 v[122:125], v[172:175], v[206:209], v[122:125]
	v_mfma_f32_16x16x32_bf16 v[94:97], v[172:175], v[214:217], v[94:97]
	v_mfma_f32_16x16x32_bf16 v[78:81], v[180:183], v[214:217], v[78:81]
	v_mfma_f32_16x16x32_bf16 v[74:77], v[180:183], v[222:225], v[74:77]
	v_mfma_f32_16x16x32_bf16 v[90:93], v[172:175], v[222:225], v[90:93]
	v_mfma_f32_16x16x32_bf16 v[126:129], v[176:179], v[202:205], v[126:129]
	v_mfma_f32_16x16x32_bf16 v[110:113], v[184:187], v[202:205], v[110:113]
	v_mfma_f32_16x16x32_bf16 v[106:109], v[184:187], v[210:213], v[106:109]
	v_mfma_f32_16x16x32_bf16 v[122:125], v[176:179], v[210:213], v[122:125]
	v_mfma_f32_16x16x32_bf16 v[94:97], v[176:179], v[218:221], v[94:97]
	v_mfma_f32_16x16x32_bf16 v[78:81], v[184:187], v[218:221], v[78:81]
	v_mfma_f32_16x16x32_bf16 v[74:77], v[184:187], v[226:229], v[74:77]
	v_mfma_f32_16x16x32_bf16 v[90:93], v[176:179], v[226:229], v[90:93]
	s_setprio 0
	s_barrier
	s_mov_b32 m0, s75
	s_or_b32 s16, s15, 0x80
	ds_read_b128 v[188:191], v171 offset:49152
	ds_read_b128 v[202:205], v171 offset:50176
	ds_read_b128 v[206:209], v171 offset:51200
	ds_read_b128 v[210:213], v171 offset:52224
	ds_read_b128 v[214:217], v171 offset:53248
	ds_read_b128 v[218:221], v171 offset:54272
	ds_read_b128 v[222:225], v171 offset:55296
	ds_read_b128 v[226:229], v171 offset:56320
	buffer_load_dwordx4 v166, s[48:51], s16 offen lds
	s_mov_b32 m0, s76
	s_add_i32 s15, s15, 0x80080
	buffer_load_dwordx4 v168, s[48:51], s16 offen lds
	s_mov_b32 m0, s79
	s_nop 0
	buffer_load_dwordx4 v166, s[48:51], s15 offen lds
	s_mov_b32 m0, s86
	s_nop 0
	buffer_load_dwordx4 v168, s[48:51], s15 offen lds
	s_mov_b32 m0, s77
	s_nop 0
	buffer_load_dwordx4 v145, s[88:91], s14 offen lds
	s_mov_b32 m0, s78
	s_nop 0
	buffer_load_dwordx4 v167, s[88:91], s14 offen lds
	s_waitcnt vmcnt(8)
	s_waitcnt lgkmcnt(0)
	s_barrier
	s_setprio 1
	s_waitcnt lgkmcnt(7)
	v_mfma_f32_16x16x32_bf16 v[54:57], v[130:133], v[188:191], v[54:57]
	v_mfma_f32_16x16x32_bf16 v[38:41], v[138:141], v[188:191], v[38:41]
	s_waitcnt lgkmcnt(5)
	v_mfma_f32_16x16x32_bf16 v[34:37], v[138:141], v[206:209], v[34:37]
	v_mfma_f32_16x16x32_bf16 v[50:53], v[130:133], v[206:209], v[50:53]
	s_waitcnt lgkmcnt(3)
	v_mfma_f32_16x16x32_bf16 v[22:25], v[130:133], v[214:217], v[22:25]
	v_mfma_f32_16x16x32_bf16 v[6:9], v[138:141], v[214:217], v[6:9]
	s_waitcnt lgkmcnt(1)
	v_mfma_f32_16x16x32_bf16 v[2:5], v[138:141], v[222:225], v[2:5]
	v_mfma_f32_16x16x32_bf16 v[18:21], v[130:133], v[222:225], v[18:21]
	v_mfma_f32_16x16x32_bf16 v[54:57], v[134:137], v[202:205], v[54:57]
	v_mfma_f32_16x16x32_bf16 v[38:41], v[150:153], v[202:205], v[38:41]
	v_mfma_f32_16x16x32_bf16 v[34:37], v[150:153], v[210:213], v[34:37]
	v_mfma_f32_16x16x32_bf16 v[50:53], v[134:137], v[210:213], v[50:53]
	v_mfma_f32_16x16x32_bf16 v[22:25], v[134:137], v[218:221], v[22:25]
	v_mfma_f32_16x16x32_bf16 v[6:9], v[150:153], v[218:221], v[6:9]
	s_waitcnt lgkmcnt(0)
	v_mfma_f32_16x16x32_bf16 v[2:5], v[150:153], v[226:229], v[2:5]
	v_mfma_f32_16x16x32_bf16 v[18:21], v[134:137], v[226:229], v[18:21]
	s_setprio 0
	s_setprio 1
	v_mfma_f32_16x16x32_bf16 v[62:65], v[172:175], v[188:191], v[62:65]
	v_mfma_f32_16x16x32_bf16 v[46:49], v[180:183], v[188:191], v[46:49]
	v_mfma_f32_16x16x32_bf16 v[42:45], v[180:183], v[206:209], v[42:45]
	v_mfma_f32_16x16x32_bf16 v[58:61], v[172:175], v[206:209], v[58:61]
	v_mfma_f32_16x16x32_bf16 v[30:33], v[172:175], v[214:217], v[30:33]
	v_mfma_f32_16x16x32_bf16 v[14:17], v[180:183], v[214:217], v[14:17]
	v_mfma_f32_16x16x32_bf16 v[10:13], v[180:183], v[222:225], v[10:13]
	v_mfma_f32_16x16x32_bf16 v[26:29], v[172:175], v[222:225], v[26:29]
	v_mfma_f32_16x16x32_bf16 v[62:65], v[176:179], v[202:205], v[62:65]
	v_mfma_f32_16x16x32_bf16 v[46:49], v[184:187], v[202:205], v[46:49]
	v_mfma_f32_16x16x32_bf16 v[42:45], v[184:187], v[210:213], v[42:45]
	v_mfma_f32_16x16x32_bf16 v[58:61], v[176:179], v[210:213], v[58:61]
	v_mfma_f32_16x16x32_bf16 v[30:33], v[176:179], v[218:221], v[30:33]
	v_mfma_f32_16x16x32_bf16 v[14:17], v[184:187], v[218:221], v[14:17]
	v_mfma_f32_16x16x32_bf16 v[10:13], v[184:187], v[226:229], v[10:13]
	v_mfma_f32_16x16x32_bf16 v[26:29], v[176:179], v[226:229], v[26:29]
	s_setprio 0
	s_barrier
	s_add_i32 s13, s13, 2
	s_addk_i32 s1, 0x100
	s_addk_i32 s12, 0x100
	s_cmp_gt_u32 s13, 29
	s_cbranch_scc0 .LBB0_330
	s_and_b64 vcc, exec, s[68:69]
	s_cbranch_vccz .LBB0_333
	s_barrier

; #define PG8_STAGEA(bufoff, soff, voff) do { _Pragma("unroll") for (int _i = 0; _i < 2; ++_i) \
;         __builtin_amdgcn_raw_ptr_buffer_load_lds(rsA, (PG8_LAS unsigned*)(lds + (bufoff) + ldsw + _i * 8192), 16, (voff)[_i], (soff), 0, 0); } while (0)
; #define PG8_STAGEB(bufoff, soff, voff) do { _Pragma("unroll") for (int _i = 0; _i < 2; ++_i) \
;         __builtin_amdgcn_raw_ptr_buffer_load_lds(rsB, (PG8_LAS unsigned*)(lds + (bufoff) + ldsw + _i * 8192), 16, (voff)[_i], (soff), 0, 0); } while (0)
; #define PG8_LDA(dst, b, h) do { _Pragma("unroll") for (int m = 0; m < 4; ++m) _Pragma("unroll") for (int k = 0; k < 2; ++k) dst[m][k] = *(const PG8_LAS bf16x8*)(lds + PG8_SA(b, h) + aoff + m * 2048 + k * 1024); } while (0)
; #define PG8_LDB(dst, b, h) do { _Pragma("unroll") for (int n = 0; n < 2; ++n) _Pragma("unroll") for (int k = 0; k < 2; ++k) dst[n][k] = *(const PG8_LAS bf16x8*)(lds + PG8_SB(b, h) + boff + n * 2048 + k * 1024); } while (0)
; #define PG8_MMA(ai, bj, At, Bt) do { __builtin_amdgcn_s_setprio(1); _Pragma("unroll") for (int m = 0; m < 4; ++m) _Pragma("unroll") for (int n = 0; n < 2; ++n) _Pragma("unroll") for (int k = 0; k < 2; ++k) \
;         acc[ai][bj][m][n] = __builtin_amdgcn_mfma_f32_16x16x32_bf16(Bt[n][k], At[m][k], acc[ai][bj][m][n], 0, 0, 0); __builtin_amdgcn_s_setprio(0); } while (0)
; #define PG8_WAIT_V(n) asm volatile("s_waitcnt vmcnt(" #n ")" ::: "memory")
; #define PG8_WAIT_L(n) asm volatile("s_waitcnt lgkmcnt(" #n ")" ::: "memory")
; #define PG8_BAR __builtin_amdgcn_s_barrier()
; #define PG8_SCHED __builtin_amdgcn_sched_barrier(0)
; template <class Epi, class Sched, bool ALIGN_EPI = false>
; __device__ __forceinline__ void gemm_phase(PG8_LAS unsigned char* lds, const Gemm g, const Sched& S, const Epi& E, const int tid) {
;     ...
;             PG8_LDB(B0, 0, 0); PG8_LDB(B1, 0, 1); PG8_SCHED; PG8_LDA(At, 0, 0); PG8_STAGEA(PG8_SA(1, 1), a1 + hstepA, voffA);
;             PG8_WAIT_V(8); PG8_WAIT_L(0); PG8_BAR; PG8_MMA(0, 0, At, B0); PG8_MMA(0, 1, At, B1); PG8_BAR; PG8_SCHED;
;             PG8_LDA(At, 0, 1); PG8_STAGEB(PG8_SB(0, 0), b2, voffB); PG8_STAGEB(PG8_SB(0, 1), b2 + hstepB, voffB); PG8_STAGEA(PG8_SA(0, 0), a2, voffA);
;             PG8_WAIT_V(8); PG8_WAIT_L(0); PG8_BAR; PG8_MMA(1, 0, At, B0); PG8_MMA(1, 1, At, B1); PG8_BAR; PG8_SCHED;
.LBB0_951:
	v_add_u32_e32 v86, 0x10000, v177
	v_add_u32_e32 v168, 0x14000, v177
	ds_read_b128 v[74:77], v86
	ds_read_b128 v[78:81], v86 offset:1024
	ds_read_b128 v[82:85], v86 offset:2048
	ds_read_b128 v[86:89], v86 offset:3072
	ds_read_b128 v[146:149], v168
	ds_read_b128 v[150:153], v168 offset:1024
	ds_read_b128 v[164:167], v168 offset:2048
	ds_read_b128 v[168:171], v168 offset:3072
	s_add_i32 s43, s28, 0x80
	s_cmp_eq_u32 s51, s42
	s_cselect_b32 s61, s56, s43
	s_cselect_b32 s60, s57, s29
	s_add_i32 s43, s61, 0x80
	s_add_i32 s46, s11, s28
	s_mov_b32 m0, s52
	ds_read_b128 v[180:183], v178
	ds_read_b128 v[184:187], v178 offset:1024
	ds_read_b128 v[188:191], v178 offset:2048
	ds_read_b128 v[202:205], v178 offset:3072
	ds_read_b128 v[206:209], v178 offset:4096
	ds_read_b128 v[210:213], v178 offset:5120
	ds_read_b128 v[214:217], v178 offset:6144
	ds_read_b128 v[218:221], v178 offset:7168
	buffer_load_dwordx4 v0, s[88:91], s46 offen lds
	s_mov_b32 m0, s53
	s_nop 0
	buffer_load_dwordx4 v173, s[88:91], s46 offen lds
	s_waitcnt vmcnt(8)
	s_waitcnt lgkmcnt(0)
	s_barrier
	s_setprio 1
	s_waitcnt lgkmcnt(7)
	v_mfma_f32_16x16x32_bf16 v[142:145], v[74:77], v[180:183], v[142:145]
	v_mfma_f32_16x16x32_bf16 v[138:141], v[82:85], v[180:183], v[138:141]
	s_waitcnt lgkmcnt(5)
	v_mfma_f32_16x16x32_bf16 v[122:125], v[82:85], v[188:191], v[122:125]
	v_mfma_f32_16x16x32_bf16 v[126:129], v[74:77], v[188:191], v[126:129]
	s_waitcnt lgkmcnt(3)
	v_mfma_f32_16x16x32_bf16 v[110:113], v[74:77], v[206:209], v[110:113]
	v_mfma_f32_16x16x32_bf16 v[106:109], v[82:85], v[206:209], v[106:109]
	s_waitcnt lgkmcnt(1)
	v_mfma_f32_16x16x32_bf16 v[90:93], v[82:85], v[214:217], v[90:93]
	v_mfma_f32_16x16x32_bf16 v[94:97], v[74:77], v[214:217], v[94:97]
	v_mfma_f32_16x16x32_bf16 v[142:145], v[78:81], v[184:187], v[142:145]
	v_mfma_f32_16x16x32_bf16 v[138:141], v[86:89], v[184:187], v[138:141]
	v_mfma_f32_16x16x32_bf16 v[122:125], v[86:89], v[202:205], v[122:125]
	v_mfma_f32_16x16x32_bf16 v[126:129], v[78:81], v[202:205], v[126:129]
	v_mfma_f32_16x16x32_bf16 v[110:113], v[78:81], v[210:213], v[110:113]
	v_mfma_f32_16x16x32_bf16 v[106:109], v[86:89], v[210:213], v[106:109]
	s_waitcnt lgkmcnt(0)
	v_mfma_f32_16x16x32_bf16 v[90:93], v[86:89], v[218:221], v[90:93]
	v_mfma_f32_16x16x32_bf16 v[94:97], v[78:81], v[218:221], v[94:97]
	s_setprio 0
	s_setprio 1
	v_mfma_f32_16x16x32_bf16 v[134:137], v[146:149], v[180:183], v[134:137]
	v_mfma_f32_16x16x32_bf16 v[130:133], v[164:167], v[180:183], v[130:133]
	v_mfma_f32_16x16x32_bf16 v[114:117], v[164:167], v[188:191], v[114:117]
	v_mfma_f32_16x16x32_bf16 v[118:121], v[146:149], v[188:191], v[118:121]
	v_mfma_f32_16x16x32_bf16 v[102:105], v[146:149], v[206:209], v[102:105]
	v_mfma_f32_16x16x32_bf16 v[98:101], v[164:167], v[206:209], v[98:101]
	v_mfma_f32_16x16x32_bf16 v[66:69], v[164:167], v[214:217], v[66:69]
	v_mfma_f32_16x16x32_bf16 v[70:73], v[146:149], v[214:217], v[70:73]
	v_mfma_f32_16x16x32_bf16 v[134:137], v[150:153], v[184:187], v[134:137]
	v_mfma_f32_16x16x32_bf16 v[130:133], v[168:171], v[184:187], v[130:133]
	v_mfma_f32_16x16x32_bf16 v[114:117], v[168:171], v[202:205], v[114:117]
	v_mfma_f32_16x16x32_bf16 v[118:121], v[150:153], v[202:205], v[118:121]
	v_mfma_f32_16x16x32_bf16 v[102:105], v[150:153], v[210:213], v[102:105]
	v_mfma_f32_16x16x32_bf16 v[98:101], v[168:171], v[210:213], v[98:101]
	v_mfma_f32_16x16x32_bf16 v[66:69], v[168:171], v[218:221], v[66:69]
	v_mfma_f32_16x16x32_bf16 v[70:73], v[150:153], v[218:221], v[70:73]
	s_setprio 0
	s_barrier
	s_mov_b32 m0, s17
	s_mov_b32 s46, s90
	s_mov_b32 s47, s91
	ds_read_b128 v[180:183], v178 offset:16384
	ds_read_b128 v[184:187], v178 offset:17408
	ds_read_b128 v[188:191], v178 offset:18432
	ds_read_b128 v[202:205], v178 offset:19456
	ds_read_b128 v[206:209], v178 offset:20480
	ds_read_b128 v[210:213], v178 offset:21504
	ds_read_b128 v[214:217], v178 offset:22528
	ds_read_b128 v[218:221], v178 offset:23552
	buffer_load_dwordx4 v172, s[44:47], s60 offen lds
	s_mov_b32 m0, s20
	s_add_i32 s62, s60, s14
	buffer_load_dwordx4 v174, s[44:47], s60 offen lds
	s_mov_b32 m0, s21
	s_nop 0
	buffer_load_dwordx4 v172, s[44:47], s62 offen lds
	s_mov_b32 m0, s24
	s_nop 0
	buffer_load_dwordx4 v174, s[44:47], s62 offen lds
	s_mov_b32 m0, s16
	s_nop 0
	buffer_load_dwordx4 v0, s[88:91], s61 offen lds
	s_mov_b32 m0, s25
	s_nop 0
	buffer_load_dwordx4 v173, s[88:91], s61 offen lds
	s_waitcnt vmcnt(8)
	s_waitcnt lgkmcnt(0)
	s_barrier
	s_setprio 1
	s_waitcnt lgkmcnt(7)
	v_mfma_f32_16x16x32_bf16 v[62:65], v[74:77], v[180:183], v[62:65]
	v_mfma_f32_16x16x32_bf16 v[58:61], v[82:85], v[180:183], v[58:61]
	s_waitcnt lgkmcnt(5)
	v_mfma_f32_16x16x32_bf16 v[42:45], v[82:85], v[188:191], v[42:45]
	v_mfma_f32_16x16x32_bf16 v[46:49], v[74:77], v[188:191], v[46:49]
	s_waitcnt lgkmcnt(3)
	v_mfma_f32_16x16x32_bf16 v[30:33], v[74:77], v[206:209], v[30:33]
	v_mfma_f32_16x16x32_bf16 v[26:29], v[82:85], v[206:209], v[26:29]
	s_waitcnt lgkmcnt(1)
	v_mfma_f32_16x16x32_bf16 v[10:13], v[82:85], v[214:217], v[10:13]
	v_mfma_f32_16x16x32_bf16 v[14:17], v[74:77], v[214:217], v[14:17]
	v_mfma_f32_16x16x32_bf16 v[62:65], v[78:81], v[184:187], v[62:65]
	v_mfma_f32_16x16x32_bf16 v[58:61], v[86:89], v[184:187], v[58:61]
	v_mfma_f32_16x16x32_bf16 v[42:45], v[86:89], v[202:205], v[42:45]
	v_mfma_f32_16x16x32_bf16 v[46:49], v[78:81], v[202:205], v[46:49]
	v_mfma_f32_16x16x32_bf16 v[30:33], v[78:81], v[210:213], v[30:33]
	v_mfma_f32_16x16x32_bf16 v[26:29], v[86:89], v[210:213], v[26:29]
	s_waitcnt lgkmcnt(0)
	v_mfma_f32_16x16x32_bf16 v[10:13], v[86:89], v[218:221], v[10:13]
	v_mfma_f32_16x16x32_bf16 v[14:17], v[78:81], v[218:221], v[14:17]
	s_setprio 0
	s_setprio 1
	v_mfma_f32_16x16x32_bf16 v[54:57], v[146:149], v[180:183], v[54:57]
	v_mfma_f32_16x16x32_bf16 v[50:53], v[164:167], v[180:183], v[50:53]
	v_mfma_f32_16x16x32_bf16 v[34:37], v[164:167], v[188:191], v[34:37]
	v_mfma_f32_16x16x32_bf16 v[38:41], v[146:149], v[188:191], v[38:41]
	v_mfma_f32_16x16x32_bf16 v[22:25], v[146:149], v[206:209], v[22:25]
	v_mfma_f32_16x16x32_bf16 v[18:21], v[164:167], v[206:209], v[18:21]
	v_mfma_f32_16x16x32_bf16 v[2:5], v[164:167], v[214:217], v[2:5]
	v_mfma_f32_16x16x32_bf16 v[6:9], v[146:149], v[214:217], v[6:9]
	v_mfma_f32_16x16x32_bf16 v[54:57], v[150:153], v[184:187], v[54:57]
	v_mfma_f32_16x16x32_bf16 v[50:53], v[168:171], v[184:187], v[50:53]
	v_mfma_f32_16x16x32_bf16 v[34:37], v[168:171], v[202:205], v[34:37]
	v_mfma_f32_16x16x32_bf16 v[38:41], v[150:153], v[202:205], v[38:41]
	v_mfma_f32_16x16x32_bf16 v[22:25], v[150:153], v[210:213], v[22:25]
	v_mfma_f32_16x16x32_bf16 v[18:21], v[168:171], v[210:213], v[18:21]
	v_mfma_f32_16x16x32_bf16 v[2:5], v[168:171], v[218:221], v[2:5]
	v_mfma_f32_16x16x32_bf16 v[6:9], v[150:153], v[218:221], v[6:9]
	s_setprio 0
	s_barrier
; #define PG8_STAGEA(bufoff, soff, voff) do { _Pragma("unroll") for (int _i = 0; _i < 2; ++_i) \
;         __builtin_amdgcn_raw_ptr_buffer_load_lds(rsA, (PG8_LAS unsigned*)(lds + (bufoff) + ldsw + _i * 8192), 16, (voff)[_i], (soff), 0, 0); } while (0)
; #define PG8_STAGEB(bufoff, soff, voff) do { _Pragma("unroll") for (int _i = 0; _i < 2; ++_i) \
;         __builtin_amdgcn_raw_ptr_buffer_load_lds(rsB, (PG8_LAS unsigned*)(lds + (bufoff) + ldsw + _i * 8192), 16, (voff)[_i], (soff), 0, 0); } while (0)
; #define PG8_LDA(dst, b, h) do { _Pragma("unroll") for (int m = 0; m < 4; ++m) _Pragma("unroll") for (int k = 0; k < 2; ++k) dst[m][k] = *(const PG8_LAS bf16x8*)(lds + PG8_SA(b, h) + aoff + m * 2048 + k * 1024); } while (0)
; #define PG8_LDB(dst, b, h) do { _Pragma("unroll") for (int n = 0; n < 2; ++n) _Pragma("unroll") for (int k = 0; k < 2; ++k) dst[n][k] = *(const PG8_LAS bf16x8*)(lds + PG8_SB(b, h) + boff + n * 2048 + k * 1024); } while (0)
; #define PG8_MMA(ai, bj, At, Bt) do { __builtin_amdgcn_s_setprio(1); _Pragma("unroll") for (int m = 0; m < 4; ++m) _Pragma("unroll") for (int n = 0; n < 2; ++n) _Pragma("unroll") for (int k = 0; k < 2; ++k) \
;         acc[ai][bj][m][n] = __builtin_amdgcn_mfma_f32_16x16x32_bf16(Bt[n][k], At[m][k], acc[ai][bj][m][n], 0, 0, 0); __builtin_amdgcn_s_setprio(0); } while (0)
; #define PG8_WAIT_V(n) asm volatile("s_waitcnt vmcnt(" #n ")" ::: "memory")
; #define PG8_WAIT_L(n) asm volatile("s_waitcnt lgkmcnt(" #n ")" ::: "memory")
; #define PG8_BAR __builtin_amdgcn_s_barrier()
; #define PG8_SCHED __builtin_amdgcn_sched_barrier(0)
; template <class Epi, class Sched, bool ALIGN_EPI = false>
; __device__ __forceinline__ void gemm_phase(PG8_LAS unsigned char* lds, const Gemm g, const Sched& S, const Epi& E, const int tid) {
;     ...
;             PG8_LDB(B0, 1, 0); PG8_LDB(B1, 1, 1); PG8_SCHED; PG8_LDA(At, 1, 0); PG8_STAGEA(PG8_SA(0, 1), a2 + hstepA, voffA);
;             PG8_WAIT_V(8); PG8_WAIT_L(0); PG8_BAR; PG8_MMA(0, 0, At, B0); PG8_MMA(0, 1, At, B1); PG8_BAR; PG8_SCHED;
;             PG8_LDA(At, 1, 1); PG8_STAGEB(PG8_SB(1, 0), b3, voffB); PG8_STAGEB(PG8_SB(1, 1), b3 + hstepB, voffB); PG8_STAGEA(PG8_SA(1, 0), a3, voffA);
;             PG8_WAIT_V(8); PG8_WAIT_L(0); PG8_BAR; PG8_MMA(1, 0, At, B0); PG8_MMA(1, 1, At, B1); PG8_BAR; PG8_SCHED;
;         }
	v_add_u32_e32 v86, 0x18000, v177
	v_add_u32_e32 v168, 0x1c000, v177
	ds_read_b128 v[74:77], v86
	ds_read_b128 v[78:81], v86 offset:1024
	ds_read_b128 v[82:85], v86 offset:2048
	ds_read_b128 v[86:89], v86 offset:3072
	ds_read_b128 v[146:149], v168
	ds_read_b128 v[150:153], v168 offset:1024
	ds_read_b128 v[164:167], v168 offset:2048
	ds_read_b128 v[168:171], v168 offset:3072
	s_add_i32 s61, s61, s11
	s_mov_b32 m0, s30
	ds_read_b128 v[180:183], v178 offset:32768
	ds_read_b128 v[184:187], v178 offset:33792
	ds_read_b128 v[188:191], v178 offset:34816
	ds_read_b128 v[202:205], v178 offset:35840
	ds_read_b128 v[206:209], v178 offset:36864
	ds_read_b128 v[210:213], v178 offset:37888
	ds_read_b128 v[214:217], v178 offset:38912
	ds_read_b128 v[218:221], v178 offset:39936
	buffer_load_dwordx4 v0, s[88:91], s61 offen lds
	s_mov_b32 m0, s31
	s_nop 0
	buffer_load_dwordx4 v173, s[88:91], s61 offen lds
	s_waitcnt vmcnt(8)
	s_waitcnt lgkmcnt(0)
	s_barrier
	s_setprio 1
	s_waitcnt lgkmcnt(7)
	v_mfma_f32_16x16x32_bf16 v[142:145], v[74:77], v[180:183], v[142:145]
	v_mfma_f32_16x16x32_bf16 v[138:141], v[82:85], v[180:183], v[138:141]
	s_waitcnt lgkmcnt(5)
	v_mfma_f32_16x16x32_bf16 v[122:125], v[82:85], v[188:191], v[122:125]
	v_mfma_f32_16x16x32_bf16 v[126:129], v[74:77], v[188:191], v[126:129]
	s_waitcnt lgkmcnt(3)
	v_mfma_f32_16x16x32_bf16 v[110:113], v[74:77], v[206:209], v[110:113]
	v_mfma_f32_16x16x32_bf16 v[106:109], v[82:85], v[206:209], v[106:109]
	s_waitcnt lgkmcnt(1)
	v_mfma_f32_16x16x32_bf16 v[90:93], v[82:85], v[214:217], v[90:93]
	v_mfma_f32_16x16x32_bf16 v[94:97], v[74:77], v[214:217], v[94:97]
	v_mfma_f32_16x16x32_bf16 v[142:145], v[78:81], v[184:187], v[142:145]
	v_mfma_f32_16x16x32_bf16 v[138:141], v[86:89], v[184:187], v[138:141]
	v_mfma_f32_16x16x32_bf16 v[122:125], v[86:89], v[202:205], v[122:125]
	v_mfma_f32_16x16x32_bf16 v[126:129], v[78:81], v[202:205], v[126:129]
	v_mfma_f32_16x16x32_bf16 v[110:113], v[78:81], v[210:213], v[110:113]
	v_mfma_f32_16x16x32_bf16 v[106:109], v[86:89], v[210:213], v[106:109]
	s_waitcnt lgkmcnt(0)
	v_mfma_f32_16x16x32_bf16 v[90:93], v[86:89], v[218:221], v[90:93]
	v_mfma_f32_16x16x32_bf16 v[94:97], v[78:81], v[218:221], v[94:97]
	s_setprio 0
	s_setprio 1
	v_mfma_f32_16x16x32_bf16 v[134:137], v[146:149], v[180:183], v[134:137]
	v_mfma_f32_16x16x32_bf16 v[130:133], v[164:167], v[180:183], v[130:133]
	v_mfma_f32_16x16x32_bf16 v[114:117], v[164:167], v[188:191], v[114:117]
	v_mfma_f32_16x16x32_bf16 v[118:121], v[146:149], v[188:191], v[118:121]
	v_mfma_f32_16x16x32_bf16 v[102:105], v[146:149], v[206:209], v[102:105]
	v_mfma_f32_16x16x32_bf16 v[98:101], v[164:167], v[206:209], v[98:101]
	v_mfma_f32_16x16x32_bf16 v[66:69], v[164:167], v[214:217], v[66:69]
	v_mfma_f32_16x16x32_bf16 v[70:73], v[146:149], v[214:217], v[70:73]
	v_mfma_f32_16x16x32_bf16 v[134:137], v[150:153], v[184:187], v[134:137]
	v_mfma_f32_16x16x32_bf16 v[130:133], v[168:171], v[184:187], v[130:133]
	v_mfma_f32_16x16x32_bf16 v[114:117], v[168:171], v[202:205], v[114:117]
	v_mfma_f32_16x16x32_bf16 v[118:121], v[150:153], v[202:205], v[118:121]
	v_mfma_f32_16x16x32_bf16 v[102:105], v[150:153], v[210:213], v[102:105]
	v_mfma_f32_16x16x32_bf16 v[98:101], v[168:171], v[210:213], v[98:101]
	v_mfma_f32_16x16x32_bf16 v[66:69], v[168:171], v[218:221], v[66:69]
	v_mfma_f32_16x16x32_bf16 v[70:73], v[150:153], v[218:221], v[70:73]
	s_setprio 0
	s_barrier
	s_mov_b32 m0, s33
	s_addk_i32 s60, 0x80
	ds_read_b128 v[180:183], v178 offset:49152
	ds_read_b128 v[184:187], v178 offset:50176
	ds_read_b128 v[188:191], v178 offset:51200
	ds_read_b128 v[202:205], v178 offset:52224
	ds_read_b128 v[206:209], v178 offset:53248
	ds_read_b128 v[210:213], v178 offset:54272
	ds_read_b128 v[214:217], v178 offset:55296
	ds_read_b128 v[218:221], v178 offset:56320
	buffer_load_dwordx4 v172, s[44:47], s60 offen lds
	s_mov_b32 m0, s34
	s_nop 0
	buffer_load_dwordx4 v174, s[44:47], s60 offen lds
	s_add_i32 s60, s60, s14
	s_mov_b32 m0, s37
	s_nop 0
	buffer_load_dwordx4 v172, s[44:47], s60 offen lds
	s_mov_b32 m0, s38
	s_nop 0
	buffer_load_dwordx4 v174, s[44:47], s60 offen lds
	s_mov_b32 m0, s35
	s_nop 0
	buffer_load_dwordx4 v0, s[88:91], s43 offen lds
	s_mov_b32 m0, s36
	s_nop 0
	buffer_load_dwordx4 v173, s[88:91], s43 offen lds
	s_waitcnt vmcnt(8)
	s_waitcnt lgkmcnt(0)
	s_barrier
	s_setprio 1
	s_waitcnt lgkmcnt(7)
	v_mfma_f32_16x16x32_bf16 v[62:65], v[74:77], v[180:183], v[62:65]
	v_mfma_f32_16x16x32_bf16 v[58:61], v[82:85], v[180:183], v[58:61]
	s_waitcnt lgkmcnt(5)
	v_mfma_f32_16x16x32_bf16 v[42:45], v[82:85], v[188:191], v[42:45]
	v_mfma_f32_16x16x32_bf16 v[46:49], v[74:77], v[188:191], v[46:49]
	s_waitcnt lgkmcnt(3)
	v_mfma_f32_16x16x32_bf16 v[30:33], v[74:77], v[206:209], v[30:33]
	v_mfma_f32_16x16x32_bf16 v[26:29], v[82:85], v[206:209], v[26:29]
	s_waitcnt lgkmcnt(1)
	v_mfma_f32_16x16x32_bf16 v[10:13], v[82:85], v[214:217], v[10:13]
	v_mfma_f32_16x16x32_bf16 v[14:17], v[74:77], v[214:217], v[14:17]
	v_mfma_f32_16x16x32_bf16 v[62:65], v[78:81], v[184:187], v[62:65]
	v_mfma_f32_16x16x32_bf16 v[58:61], v[86:89], v[184:187], v[58:61]
	v_mfma_f32_16x16x32_bf16 v[42:45], v[86:89], v[202:205], v[42:45]
	v_mfma_f32_16x16x32_bf16 v[46:49], v[78:81], v[202:205], v[46:49]
	v_mfma_f32_16x16x32_bf16 v[30:33], v[78:81], v[210:213], v[30:33]
	v_mfma_f32_16x16x32_bf16 v[26:29], v[86:89], v[210:213], v[26:29]
	s_waitcnt lgkmcnt(0)
	v_mfma_f32_16x16x32_bf16 v[10:13], v[86:89], v[218:221], v[10:13]
	v_mfma_f32_16x16x32_bf16 v[14:17], v[78:81], v[218:221], v[14:17]
	s_setprio 0
	s_setprio 1
	v_mfma_f32_16x16x32_bf16 v[54:57], v[146:149], v[180:183], v[54:57]
	v_mfma_f32_16x16x32_bf16 v[50:53], v[164:167], v[180:183], v[50:53]
	v_mfma_f32_16x16x32_bf16 v[34:37], v[164:167], v[188:191], v[34:37]
	v_mfma_f32_16x16x32_bf16 v[38:41], v[146:149], v[188:191], v[38:41]
	v_mfma_f32_16x16x32_bf16 v[22:25], v[146:149], v[206:209], v[22:25]
	v_mfma_f32_16x16x32_bf16 v[18:21], v[164:167], v[206:209], v[18:21]
	v_mfma_f32_16x16x32_bf16 v[2:5], v[164:167], v[214:217], v[2:5]
	v_mfma_f32_16x16x32_bf16 v[6:9], v[146:149], v[214:217], v[6:9]
	v_mfma_f32_16x16x32_bf16 v[54:57], v[150:153], v[184:187], v[54:57]
	v_mfma_f32_16x16x32_bf16 v[50:53], v[168:171], v[184:187], v[50:53]
	v_mfma_f32_16x16x32_bf16 v[34:37], v[168:171], v[202:205], v[34:37]
	v_mfma_f32_16x16x32_bf16 v[38:41], v[150:153], v[202:205], v[38:41]
	v_mfma_f32_16x16x32_bf16 v[22:25], v[150:153], v[210:213], v[22:25]
	v_mfma_f32_16x16x32_bf16 v[18:21], v[168:171], v[210:213], v[18:21]
	v_mfma_f32_16x16x32_bf16 v[2:5], v[168:171], v[218:221], v[2:5]
	v_mfma_f32_16x16x32_bf16 v[6:9], v[150:153], v[218:221], v[6:9]
	s_setprio 0
	s_barrier
	s_add_i32 s42, s42, 2
	s_addk_i32 s28, 0x100
	s_addk_i32 s29, 0x100
	s_cmp_ge_u32 s42, s50
	s_cbranch_scc0 .LBB0_951
	s_and_b64 vcc, exec, s[4:5]
	s_cbranch_vccz .LBB0_954
	s_barrier
